# MLA attention loop: counted LDS waits in the P.V section (each MFMA waits only for its own two V fragments) and one static priority raise for waves 4-7 during the phase
# speedup vs baseline: 1.0112x; 1.0046x over previous
; #define LAS __attribute__((address_space(3)))
; __device__ __forceinline__ int v_st(int k, int c) { const int kk = (k & ~0xC) | ((k & 4) << 1) | ((k & 8) >> 1); return ((kk >> 3) * 4 + (c >> 5)) * 512 + ((kk & 7) * 32 + (c & 31)) * 2; }
; __device__ __forceinline__ int v_rd_base(int lane) { return ((lane & 3) << 3) | (((lane >> 2) & 3) << 6) | (((lane >> 4) & 1) << 5) | (((lane >> 5) & 1) << 8); }
; __device__ __forceinline__ void mla_attn_phase(LAS unsigned char* lds, const bf16* Q, const bf16* KV, const bf16* Z, bf16* Oabc, const float* ropec, const float* ropes, int vcu, int G, int tid) {
;     ...
;     const int wid = __builtin_amdgcn_readfirstlane(tid >> 6), lane = tid & 63, r32 = lane & 31, hi = lane >> 5;
;     constexpr int SHM_K = 64 * 384, SHM_V = 16384;
;     LAS unsigned char* K_lds = lds; LAS unsigned char* V_lds = lds + 2 * SHM_K;
;     LAS float* wsf = (LAS float*)(lds + 2 * SHM_K + 2 * SHM_V) + wid * 64; LAS float* li_l = wsf; LAS float* al_l = wsf + 32;
;     LAS unsigned char* qrl = lds + 86016 + wid * 4096;
;     const int sr = tid >> 4, sc = (tid & 15) * 8, vst0 = v_st(sr, sc);
;     const int kr_row = tid >> 3, kr_c = (tid & 7) * 8;
;     const int kst0 = KSWZ192(sr, sc * 2), kst2 = KSWZ192(kr_row, 256 + kr_c * 2);
;     const int vb0 = (int)(uintptr_t)V_lds + v_rd_base(lane);
;     int ka[4];
; #pragma unroll
;     for (int j = 0; j < 4; ++j) ka[j] = r32 * 384 + (((j * 2 + hi) ^ (r32 & 7)) << 4);
;     constexpr float SCALE = 0.07216878364870322f, C = SCALE * 1.4426950408889634f, THRS = 8.0f / SCALE;
;     const unsigned qoff = (unsigned)(((wid * 32 + r32) * 1536 + hi * 8) * 2), roff = (unsigned)(((wid * 32 + r32) * 32 + hi * 8) * 4);
;     const unsigned kvoff = (unsigned)((sr * 2048 + sc) * 2), zoff = (unsigned)((kr_row * NABC + ZC_CKR + kr_c) * 2);
.LBB0_1119:
	v_readlane_b32 s12, v252, 6
	v_readlane_b32 s8, v252, 4
	v_readlane_b32 s18, v252, 12
	v_readlane_b32 s19, v252, 13
	v_readlane_b32 s9, v252, 5
	s_mov_b64 s[6:7], s[18:19]
	v_mbcnt_lo_u32_b32 v0, -1, 0
	v_mbcnt_hi_u32_b32 v0, -1, v0
	v_readlane_b32 s0, v252, 37
	s_nop 3
	s_cmpk_lt_u32 s0, 0x100
	s_cbranch_scc1 .Lmla_prio_done
	s_setprio 1
.Lmla_prio_done:
	v_mbcnt_lo_u32_b32 v0, -1, 0
	v_mbcnt_hi_u32_b32 v0, -1, v0
	v_readlane_b32 s13, v252, 7
	v_readlane_b32 s14, v252, 8
	v_add_u32_e32 v0, s0, v0
	v_readlane_b32 s0, v252, 48
	v_readlane_b32 s1, v252, 49
	s_and_b64 vcc, exec, s[0:1]
	v_readfirstlane_b32 s4, v0
	v_readlane_b32 s15, v252, 9
	v_readlane_b32 s16, v252, 10
	v_readlane_b32 s17, v252, 11
	s_cbranch_vccz .LBB0_1138
	s_add_u32 s0, s8, 0x2fe00000
	s_addc_u32 s1, s9, 0
	s_add_u32 s18, s6, 0x4000000
	s_addc_u32 s19, s7, 0
	v_lshlrev_b32_e32 v5, 3, v0
	v_ashrrev_i32_e32 v7, 3, v0
	s_add_u32 s20, s8, 0x100000
	v_and_b32_e32 v8, 56, v5
	s_movk_i32 s10, 0x180
	v_mov_b32_e32 v11, 0x100
	v_lshlrev_b32_e32 v12, 4, v7
	s_addc_u32 s21, s9, 0
	v_and_b32_e32 v2, 31, v0
	v_bfe_u32 v3, v0, 5, 1
	v_mul_lo_u32 v10, v7, s10
	v_lshl_or_b32 v11, v8, 1, v11
	v_and_b32_e32 v12, 0x70, v12
	s_add_u32 s22, s8, 0x180000
	v_xad_u32 v199, v11, v12, v10
	v_mul_u32_u24_e32 v10, 0x180, v2
	v_and_b32_e32 v11, 7, v0
	v_bitop3_b32 v12, v3, v0, 7 bitop3:0x78
	s_addc_u32 s23, s9, 0
	s_ashr_i32 s5, s4, 6
	v_lshl_or_b32 v200, v12, 4, v10
	v_bitop3_b32 v12, v3, v11, 2 bitop3:0x36
	v_ashrrev_i32_e32 v4, 4, v0
	v_and_b32_e32 v6, 0x78, v5
	v_lshl_or_b32 v201, v12, 4, v10
	v_bitop3_b32 v12, v3, v11, 4 bitop3:0x36
	v_bitop3_b32 v11, v3, v11, 6 bitop3:0x36
	s_lshl_b32 s24, s5, 5
	v_lshlrev_b32_e32 v6, 1, v6
	v_and_b32_e32 v9, 0x70, v0
	v_lshl_or_b32 v202, v12, 4, v10
	v_lshl_or_b32 v203, v11, 4, v10
	v_mul_lo_u32 v10, v4, s10
	v_or_b32_e32 v205, s24, v2
	v_xad_u32 v204, v6, v9, v10
	v_lshlrev_b32_e32 v206, 4, v3
	v_mul_lo_u32 v9, v205, s92
	v_or_b32_e32 v207, v9, v206
	v_and_b32_e32 v9, 32, v0
	v_and_b32_e32 v198, 63, v0
	v_lshl_or_b32 v208, v205, 7, v9
	v_lshlrev_b32_e32 v9, 1, v0
	v_lshlrev_b32_e32 v0, 1, v4
	v_and_b32_e32 v11, 0xfffff0, v4
	v_and_or_b32 v0, v0, 8, v11
	s_and_b32 s4, s4, 0x3fffffc0
	v_lshrrev_b32_e32 v0, 1, v0
	v_bfe_u32 v11, v5, 5, 2
	s_lshl_b32 s4, s4, 2
	v_or_b32_e32 v11, v0, v11
	v_lshrrev_b32_e32 v0, 1, v4
	v_and_b32_e32 v12, 3, v4
	s_add_i32 s26, s4, 0
	v_and_or_b32 v0, v0, 4, v12
	s_movk_i32 s4, 0x1100
	v_lshlrev_b32_e32 v12, 6, v0
	v_mul_lo_u32 v0, v7, s4
	v_or_b32_e32 v0, v0, v8
	v_mov_b32_e32 v7, 0x2000
	s_add_i32 s26, s26, 0x14000
	v_and_b32_e32 v13, 48, v6
	v_lshl_add_u32 v0, v0, 1, v7
	v_lshl_or_b32 v164, v4, 12, v6
	v_lshl_add_u32 v4, v11, 9, 0
	v_lshlrev_b32_e32 v209, 4, v198
	v_add3_u32 v210, v4, v12, v13
	v_and_b32_e32 v4, 0x118, v5
	v_lshlrev_b32_e32 v211, 2, v3
	v_lshl_add_u32 v212, v2, 2, s26
	v_lshl_add_u64 v[2:3], s[8:9], 0, v[0:1]
	s_mov_b64 s[10:11], 0x15600000
	v_and_b32_e32 v10, 0xc0, v209
	v_lshl_add_u64 v[166:167], v[2:3], 0, s[10:11]
	v_and_or_b32 v0, v9, 32, v4
	s_add_i32 s10, 0, 0xc000
	v_mov_b32_e32 v165, v1
	v_add3_u32 v213, v10, s10, v0
	s_mov_b64 s[10:11], 0x15688000
	s_lshl_b32 s5, s5, 12
	v_lshl_add_u64 v[168:169], v[2:3], 0, s[10:11]
	v_lshl_add_u64 v[2:3], s[6:7], 0, v[164:165]
	s_mov_b64 s[6:7], 0x4040000
	s_add_i32 s25, s5, 0
	v_lshl_add_u64 v[170:171], v[2:3], 0, s[6:7]
	v_readlane_b32 s6, v254, 12
	s_add_i32 s25, s25, 0x15000
	v_cmp_gt_u32_e64 s[4:5], 32, v198
	s_ashr_i32 s27, s24, 31
	s_mov_b32 s28, s6
	v_readlane_b32 s7, v254, 13
	s_branch .LBB0_1122

; #define FA_SBAR() __builtin_amdgcn_sched_barrier(0)
; __device__ __forceinline__ void finishSM(f32x16& p0, f32x16& p1, float alpha, float& l_reg, bf16x8& pa0, bf16x8& pa1, bf16x8& pa2, bf16x8& pa3) {
; #pragma unroll
;   for (int r = 0; r < 16; ++r) p1[r] = __builtin_amdgcn_exp2f(p1[r]);
;   float ps = 0;
; #pragma unroll
;   for (int r = 0; r < 16; ++r) ps += p0[r];
; #pragma unroll
;   for (int r = 0; r < 16; ++r) ps += p1[r];
;   { auto rr = __builtin_amdgcn_permlane32_swap(__float_as_uint(ps), __float_as_uint(ps), false, false);
;     ps = __uint_as_float(rr[0]) + __uint_as_float(rr[1]); }
;   l_reg = l_reg * alpha + ps;
;   FA_PK4(p0, 0, pa0); FA_PK4(p0, 8, pa1); FA_PK4(p1, 0, pa2); FA_PK4(p1, 8, pa3);
; }
; __device__ __forceinline__ int v_st(int k, int c) { const int kk = (k & ~0xC) | ((k & 4) << 1) | ((k & 8) >> 1); return ((kk >> 3) * 4 + (c >> 5)) * 512 + ((kk & 7) * 32 + (c & 31)) * 2; }
; __device__ __forceinline__ int v_rd_base(int lane) { return ((lane & 3) << 3) | (((lane >> 2) & 3) << 6) | (((lane >> 4) & 1) << 5) | (((lane >> 5) & 1) << 8); }
; template <int OFF> __device__ __forceinline__ s16x4 tr_read(int vb) {
;   s16x4 r; asm volatile("ds_read_b64_tr_b16 %0, %1 offset:%2" : "=&v"(r) : "v"(vb), "i"(OFF) : "memory"); return r;
; }
;   s16x4 l0 = tr_read<BASE + v_rd_off(D0, 0, 0)>(vb), h0 = tr_read<BASE + v_rd_off(D0, 0, 1)>(vb), l1 = tr_read<BASE + v_rd_off(D0, 1, 0)>(vb), h1 = tr_read<BASE + v_rd_off(D0, 1, 1)>(vb);
;   s16x4 l2 = tr_read<BASE + v_rd_off(D0, 2, 0)>(vb), h2 = tr_read<BASE + v_rd_off(D0, 2, 1)>(vb), l3 = tr_read<BASE + v_rd_off(D0, 3, 0)>(vb), h3 = tr_read<BASE + v_rd_off(D0, 3, 1)>(vb);
;   asm volatile("s_waitcnt lgkmcnt(0)" : "+v"(l0), "+v"(h0), "+v"(l1), "+v"(h1), "+v"(l2), "+v"(h2), "+v"(l3), "+v"(h3) :: "memory"); FA_SBAR();
;     ...
;   od = __builtin_amdgcn_mfma_f32_32x32x16_bf16(pa0, FA_PK(l0, h0), od, 0, 0, 0);
;   od = __builtin_amdgcn_mfma_f32_32x32x16_bf16(pa1, FA_PK(l1, h1), od, 0, 0, 0);
;   od = __builtin_amdgcn_mfma_f32_32x32x16_bf16(pa2, FA_PK(l2, h2), od, 0, 0, 0);
;   od = __builtin_amdgcn_mfma_f32_32x32x16_bf16(pa3, FA_PK(l3, h3), od, 0, 0, 0);
;     ...
; }
.LBB0_1133:
	v_cndmask_b32_e64 v216, v2, v216, s[6:7]
	v_mul_f32_e32 v2, 0xbdd53b94, v216
	v_fmamk_f32 v3, v96, 0x3dd53b94, v2
	v_fmamk_f32 v4, v97, 0x3dd53b94, v2
	v_exp_f32_e32 v3, v3
	v_fmamk_f32 v5, v98, 0x3dd53b94, v2
	v_exp_f32_e32 v4, v4
	v_fmamk_f32 v6, v99, 0x3dd53b94, v2
	v_exp_f32_e32 v5, v5
	v_fmamk_f32 v7, v100, 0x3dd53b94, v2
	v_fmamk_f32 v8, v101, 0x3dd53b94, v2
	v_fmamk_f32 v9, v102, 0x3dd53b94, v2
	v_fmamk_f32 v10, v103, 0x3dd53b94, v2
	v_fmamk_f32 v11, v104, 0x3dd53b94, v2
	v_fmamk_f32 v12, v105, 0x3dd53b94, v2
	v_fmamk_f32 v13, v106, 0x3dd53b94, v2
	v_fmamk_f32 v14, v107, 0x3dd53b94, v2
	v_fmamk_f32 v15, v108, 0x3dd53b94, v2
	v_fmamk_f32 v96, v109, 0x3dd53b94, v2
	v_fmamk_f32 v97, v110, 0x3dd53b94, v2
	v_fmamk_f32 v98, v111, 0x3dd53b94, v2
	v_fmamk_f32 v80, v80, 0x3dd53b94, v2
	v_fmamk_f32 v81, v81, 0x3dd53b94, v2
	v_fmamk_f32 v82, v82, 0x3dd53b94, v2
	v_fmamk_f32 v83, v83, 0x3dd53b94, v2
	v_fmamk_f32 v84, v84, 0x3dd53b94, v2
	v_fmamk_f32 v85, v85, 0x3dd53b94, v2
	v_fmamk_f32 v86, v86, 0x3dd53b94, v2
	v_fmamk_f32 v87, v87, 0x3dd53b94, v2
	v_fmamk_f32 v88, v88, 0x3dd53b94, v2
	v_fmamk_f32 v89, v89, 0x3dd53b94, v2
	v_fmamk_f32 v90, v90, 0x3dd53b94, v2
	v_fmamk_f32 v91, v91, 0x3dd53b94, v2
	v_fmamk_f32 v92, v92, 0x3dd53b94, v2
	v_fmamk_f32 v93, v93, 0x3dd53b94, v2
	v_fmamk_f32 v94, v94, 0x3dd53b94, v2
	v_fmac_f32_e32 v2, 0x3dd53b94, v95
	v_exp_f32_e32 v95, v6
	v_exp_f32_e32 v99, v7
	v_exp_f32_e32 v100, v2
	v_add_f32_e32 v2, 0, v3
	v_exp_f32_e32 v8, v8
	v_add_f32_e32 v2, v4, v2
	v_exp_f32_e32 v9, v9
	v_add_f32_e32 v2, v5, v2
	v_exp_f32_e32 v10, v10
	v_add_f32_e32 v2, v95, v2
	v_exp_f32_e32 v11, v11
	v_add_f32_e32 v2, v99, v2
	v_exp_f32_e32 v12, v12
	v_add_f32_e32 v2, v8, v2
	v_exp_f32_e32 v13, v13
	v_add_f32_e32 v2, v9, v2
	v_exp_f32_e32 v14, v14
	v_add_f32_e32 v2, v10, v2
	v_exp_f32_e32 v15, v15
	v_add_f32_e32 v2, v11, v2
	v_exp_f32_e32 v96, v96
	v_add_f32_e32 v2, v12, v2
	v_exp_f32_e32 v97, v97
	v_add_f32_e32 v2, v13, v2
	v_exp_f32_e32 v98, v98
	v_add_f32_e32 v2, v14, v2
	v_exp_f32_e32 v80, v80
	v_add_f32_e32 v2, v15, v2
	v_exp_f32_e32 v81, v81
	v_add_f32_e32 v2, v96, v2
	v_exp_f32_e32 v82, v82
	v_add_f32_e32 v2, v97, v2
	v_exp_f32_e32 v83, v83
	v_add_f32_e32 v2, v98, v2
	v_exp_f32_e32 v84, v84
	v_add_f32_e32 v2, v80, v2
	v_exp_f32_e32 v85, v85
	v_add_f32_e32 v2, v81, v2
	v_exp_f32_e32 v86, v86
	v_add_f32_e32 v2, v82, v2
	v_exp_f32_e32 v87, v87
	v_add_f32_e32 v2, v83, v2
	v_exp_f32_e32 v88, v88
	v_add_f32_e32 v2, v84, v2
	v_exp_f32_e32 v89, v89
	v_add_f32_e32 v2, v85, v2
	v_exp_f32_e32 v90, v90
	v_add_f32_e32 v2, v86, v2
	v_exp_f32_e32 v91, v91
	v_add_f32_e32 v2, v87, v2
	v_exp_f32_e32 v92, v92
	v_add_f32_e32 v2, v88, v2
	v_exp_f32_e32 v93, v93
	v_add_f32_e32 v2, v89, v2
	v_exp_f32_e32 v94, v94
	v_add_f32_e32 v2, v90, v2
	v_add_f32_e32 v2, v91, v2
	v_add_f32_e32 v2, v92, v2
	v_add_f32_e32 v2, v93, v2
	v_add_f32_e32 v2, v94, v2
	v_add_f32_e32 v6, v100, v2
	v_mov_b32_e32 v7, v6
	s_nop 1
	v_permlane32_swap_b32_e32 v6, v7
	v_cvt_pk_bf16_f32 v2, v3, v4
	v_cvt_pk_bf16_f32 v3, v5, v95
	v_cvt_pk_bf16_f32 v4, v99, v8
	v_cvt_pk_bf16_f32 v5, v9, v10
	v_cvt_pk_bf16_f32 v8, v11, v12
	v_cvt_pk_bf16_f32 v9, v13, v14
	v_cvt_pk_bf16_f32 v10, v15, v96
	v_cvt_pk_bf16_f32 v11, v97, v98
	v_cvt_pk_bf16_f32 v12, v80, v81
	v_cvt_pk_bf16_f32 v13, v82, v83
	v_cvt_pk_bf16_f32 v14, v84, v85
	v_cvt_pk_bf16_f32 v15, v86, v87
	v_cvt_pk_bf16_f32 v80, v88, v89
	v_cvt_pk_bf16_f32 v81, v90, v91
	v_cvt_pk_bf16_f32 v82, v92, v93
	v_cvt_pk_bf16_f32 v83, v94, v100
	s_nop 0
	v_permlane32_swap_b32_e32 v2, v4
	v_permlane32_swap_b32_e32 v3, v5
	v_permlane32_swap_b32_e32 v8, v10
	v_permlane32_swap_b32_e32 v9, v11
	v_permlane32_swap_b32_e32 v12, v14
	v_permlane32_swap_b32_e32 v13, v15
	v_permlane32_swap_b32_e32 v80, v82
	v_permlane32_swap_b32_e32 v81, v83
	v_lshl_add_u32 v100, s51, 14, v213
	ds_read_b64_tr_b16 v[84:85], v100 offset:0
	ds_read_b64_tr_b16 v[86:87], v100 offset:0x800
	ds_read_b64_tr_b16 v[88:89], v100 offset:0x1000
	ds_read_b64_tr_b16 v[90:91], v100 offset:0x1800
	ds_read_b64_tr_b16 v[92:93], v100 offset:0x2000
	ds_read_b64_tr_b16 v[94:95], v100 offset:0x2800
	ds_read_b64_tr_b16 v[96:97], v100 offset:0x3000
	ds_read_b64_tr_b16 v[98:99], v100 offset:0x3800
	s_nop 0
	s_waitcnt lgkmcnt(6)
	s_nop 0
	v_mfma_f32_32x32x16_bf16 v[64:79], v[2:5], v[84:87], v[64:79]
	ds_read_b64_tr_b16 v[84:85], v100 offset:0x200
	ds_read_b64_tr_b16 v[86:87], v100 offset:0xa00
	s_waitcnt lgkmcnt(6)
	v_mfma_f32_32x32x16_bf16 v[64:79], v[8:11], v[88:91], v[64:79]
	ds_read_b64_tr_b16 v[88:89], v100 offset:0x1200
	ds_read_b64_tr_b16 v[90:91], v100 offset:0x1a00
	s_waitcnt lgkmcnt(6)
	v_mfma_f32_32x32x16_bf16 v[64:79], v[12:15], v[92:95], v[64:79]
	ds_read_b64_tr_b16 v[92:93], v100 offset:0x2200
	ds_read_b64_tr_b16 v[94:95], v100 offset:0x2a00
	s_waitcnt lgkmcnt(6)
	v_mfma_f32_32x32x16_bf16 v[64:79], v[80:83], v[96:99], v[64:79]
	ds_read_b64_tr_b16 v[96:97], v100 offset:0x3200
	ds_read_b64_tr_b16 v[98:99], v100 offset:0x3a00
	s_nop 0
	s_waitcnt lgkmcnt(6)
	s_nop 0
	v_mfma_f32_32x32x16_bf16 v[48:63], v[2:5], v[84:87], v[48:63]
	ds_read_b64_tr_b16 v[84:85], v100 offset:0x400
	ds_read_b64_tr_b16 v[86:87], v100 offset:0xc00
	s_waitcnt lgkmcnt(6)
	v_mfma_f32_32x32x16_bf16 v[48:63], v[8:11], v[88:91], v[48:63]
	ds_read_b64_tr_b16 v[88:89], v100 offset:0x1400
	ds_read_b64_tr_b16 v[90:91], v100 offset:0x1c00
	s_waitcnt lgkmcnt(6)
	v_mfma_f32_32x32x16_bf16 v[48:63], v[12:15], v[92:95], v[48:63]
	ds_read_b64_tr_b16 v[92:93], v100 offset:0x2400
	ds_read_b64_tr_b16 v[94:95], v100 offset:0x2c00
	s_waitcnt lgkmcnt(6)
	v_mfma_f32_32x32x16_bf16 v[48:63], v[80:83], v[96:99], v[48:63]
	ds_read_b64_tr_b16 v[96:97], v100 offset:0x3400
	ds_read_b64_tr_b16 v[98:99], v100 offset:0x3c00
	s_nop 0
	s_waitcnt lgkmcnt(6)
	s_nop 0
	v_mfma_f32_32x32x16_bf16 v[32:47], v[2:5], v[84:87], v[32:47]
	ds_read_b64_tr_b16 v[84:85], v100 offset:0x600
	ds_read_b64_tr_b16 v[86:87], v100 offset:0xe00
	s_waitcnt lgkmcnt(6)
	v_mfma_f32_32x32x16_bf16 v[32:47], v[8:11], v[88:91], v[32:47]
	ds_read_b64_tr_b16 v[88:89], v100 offset:0x1600
	ds_read_b64_tr_b16 v[90:91], v100 offset:0x1e00
	s_waitcnt lgkmcnt(6)
	v_mfma_f32_32x32x16_bf16 v[32:47], v[12:15], v[92:95], v[32:47]
	ds_read_b64_tr_b16 v[92:93], v100 offset:0x2600
	ds_read_b64_tr_b16 v[94:95], v100 offset:0x2e00
	s_waitcnt lgkmcnt(6)
	v_mfma_f32_32x32x16_bf16 v[32:47], v[80:83], v[96:99], v[32:47]
	ds_read_b64_tr_b16 v[96:97], v100 offset:0x3600
	ds_read_b64_tr_b16 v[98:99], v100 offset:0x3e00
	s_nop 0
	s_waitcnt lgkmcnt(6)
	s_nop 0
	v_mfma_f32_32x32x16_bf16 v[16:31], v[2:5], v[84:87], v[16:31]
	s_andn2_b64 vcc, exec, s[14:15]
	s_waitcnt lgkmcnt(4)
	v_mfma_f32_32x32x16_bf16 v[16:31], v[8:11], v[88:91], v[16:31]
	s_waitcnt lgkmcnt(2)
	v_mfma_f32_32x32x16_bf16 v[16:31], v[12:15], v[92:95], v[16:31]
	s_waitcnt lgkmcnt(0)
	v_mfma_f32_32x32x16_bf16 v[16:31], v[80:83], v[96:99], v[16:31]
	s_cbranch_vccnz .LBB0_1135
; #define MLA_SWRITE(bb) do { *(LAS v4u*)(V_lds + (bb) * SHM_V + vst0) = vs0; *(LAS v4u*)(V_lds + (bb) * SHM_V + vst0 + 8192) = vs1; \
;             *(LAS v4u*)(K_lds + (bb) * SHM_K + kst0) = ks0; *(LAS v4u*)(K_lds + (bb) * SHM_K + kst0 + 32 * 384) = ks1; \
;             *(LAS v4u*)(K_lds + (bb) * SHM_K + kst2) = krr; } while (0)
; __device__ __forceinline__ void mla_attn_phase(LAS unsigned char* lds, const bf16* Q, const bf16* KV, const bf16* Z, bf16* Oabc, const float* ropec, const float* ropes, int vcu, int G, int tid) {
;     ...
;                 if (t + 1 < nt) MLA_SWRITE(buf ^ 1);
	s_xor_b32 s6, s51, 1
	v_lshl_add_u32 v2, s6, 14, v210
	s_mulk_i32 s6, 0x6000
	s_add_i32 s6, s6, 0
	s_waitcnt vmcnt(3)
	ds_write_b128 v2, v[148:151] offset:49152
	s_waitcnt vmcnt(1)
	ds_write_b128 v2, v[156:159] offset:57344
	v_add_u32_e32 v2, s6, v204
	ds_write_b128 v2, v[144:147]
	ds_write_b128 v2, v[152:155] offset:12288
	v_add_u32_e32 v2, s6, v199
	s_waitcnt vmcnt(0)
	ds_write_b128 v2, v[160:163]

; #define PG8_BAR __builtin_amdgcn_s_barrier()
; template <class Epi, class Sched, bool ALIGN_EPI, bool F8 = false>
; __device__ __forceinline__ void gemm_phase(PG8_LAS unsigned char* lds, const Gemm g, const Sched& S, const Epi& E, int tid) {
;     ...
;     const int wid = __builtin_amdgcn_readfirstlane(tid >> 6), lane = tid & 63, wr = wid >> 2, wc = wid & 3, fr = lane & 15, fq = lane >> 4;
;     const int nt = g.K / BK;
;     unsigned voffA[2], voffB[2];
; #pragma unroll
;     for (int i = 0; i < 2; ++i) { int R, C; stage_rc(tid * 16 + i * 8192, R, C); const int Rb = Epi::PERM ? ((R & ~31) + perm32(R & 31)) : R;
;         voffA[i] = (unsigned)(R * g.lda + C) * 2u; voffB[i] = (unsigned)(Rb * g.ldb + C) * 2u; }
;     const size_t kstep = (size_t)(BK * 2);
;     const size_t hstepA = (size_t)HALF * g.lda * 2, hstepB = (size_t)HALF * g.ldb * 2;
;     const unsigned ldsw = (unsigned)wid * 1024u;
;     const int aoff = lds_byte(wr * 64 + fr, fq * 8), boff = lds_byte(wc * 32 + fr, fq * 8);
;     ...
;     Unit cur, nxt; int ui = 0;
;     if (!S.next(0, cur)) return;
;     f32x4 acc[2][2][4][2];
; #pragma unroll
;     for (int a = 0; a < 2; ++a)
; #pragma unroll
;         for (int b = 0; b < 2; ++b)
; #pragma unroll
;             for (int m = 0; m < 4; ++m)
; #pragma unroll
;                 for (int n = 0; n < 2; ++n) acc[a][b][m][n] = (f32x4){0.f, 0.f, 0.f, 0.f};
;     bf16x8 At[4][2], B0[2][2], B1[2][2]; i32x8 At8[4], B08[2], B18[2];
;     const char* cA = (const char*)g.A + cur.aoff + (size_t)cur.pm * 2 * hstepA + (size_t)cur.ka * 2; const char* cB = (const char*)g.Bt + cur.boff + (size_t)cur.pn * 2 * hstepB + (size_t)cur.kb * 2;
;     S.a_ready(cur);
;     PG8_STAGE(PG8_SB(0, 0), cB, voffB); PG8_STAGE(PG8_SB(0, 1), cB + hstepB, voffB); PG8_STAGE(PG8_SA(0, 0), cA, voffA); PG8_STAGE(PG8_SA(0, 1), cA + hstepA, voffA);
;     if (wr == 1) PG8_BAR;
;     PG8_WAIT_V(2); PG8_BAR;
;     PG8_STAGE(PG8_SB(1, 0), cB + kstep, voffB); PG8_STAGE(PG8_SA(1, 0), cA + kstep, voffA); PG8_STAGE(PG8_SB(1, 1), cB + hstepB + kstep, voffB);
;     PG8_WAIT_V(6); PG8_BAR;
; __global__ void __launch_bounds__(NWAVES * 64, 2) fwd_kernel(Args args) {
;     ...
;             __syncthreads();
;             { BODY_LOCALS pg8::Gemm g2{WSP(WS_MEMKV), WSP(WS_WXQ), 4096, D, 512}; pg8::KwOrder S2{G, bx}; pg8::EpiXW E2{WSP(WS_KW), 0};
;               pg8::gemm_phase<pg8::EpiXW, pg8::KwOrder, true>(ring, g2, S2, E2, tid); }
.LBB0_1138:
	s_setprio 0
	s_barrier
	v_mbcnt_lo_u32_b32 v0, -1, 0
	v_mbcnt_hi_u32_b32 v0, -1, v0
	v_readlane_b32 s0, v252, 37
	v_readlane_b32 s4, v252, 50
	v_readlane_b32 s5, v252, 51
	v_add_u32_e32 v0, s0, v0
	s_add_u32 s0, s8, 0x32e00000
	s_addc_u32 s1, s9, 0
	s_andn2_b64 vcc, exec, s[4:5]
	v_readfirstlane_b32 s6, v0
	s_cbranch_vccnz .LBB0_1154
	v_lshlrev_b32_e32 v2, 4, v0
	v_add_u32_e32 v3, 0x2000, v2
	v_ashrrev_i32_e32 v4, 31, v3
	v_lshrrev_b32_e32 v4, 22, v4
	v_add_u32_e32 v4, v3, v4
	v_ashrrev_i32_e32 v10, 10, v4
	v_mul_i32_i24_e32 v4, 0x400, v10
	v_sub_u32_e32 v3, v3, v4
	v_lshrrev_b32_e32 v4, 4, v3
	v_bitop3_b32 v3, v4, v3, 32 bitop3:0x6c
	v_ashrrev_i32_e32 v4, 31, v3
	v_lshrrev_b32_e32 v4, 26, v4
	v_add_u32_e32 v4, v3, v4
	v_lshlrev_b32_e32 v5, 3, v10
	v_ashrrev_i32_e32 v11, 6, v4
	v_and_b32_e32 v5, -16, v5
	v_add_u32_e32 v5, v11, v5
	v_and_b32_e32 v6, 3, v11
	s_mov_b32 s4, 0xfffe0
	v_lshrrev_b32_e32 v7, 2, v5
	v_lshlrev_b32_e32 v8, 1, v5
	v_and_b32_e32 v4, 0xc0, v4
	v_and_or_b32 v6, v5, s4, v6
	v_and_b32_e32 v7, 4, v7
	v_and_b32_e32 v8, 24, v8
	v_sub_u32_e32 v3, v3, v4
	v_or3_b32 v6, v6, v7, v8
	v_lshlrev_b32_e32 v7, 5, v10
	v_ashrrev_i16_sdwa v3, v224, sext(v3) dst_sel:DWORD dst_unused:UNUSED_PAD src0_sel:DWORD src1_sel:BYTE_0
	v_and_b32_e32 v7, 32, v7
	v_bfe_i32 v12, v3, 0, 16
	v_add_lshl_u32 v3, v7, v12, 1
	v_lshl_add_u32 v130, v6, 12, v3
	v_lshl_add_u32 v132, v5, 13, v3
	v_bfe_i32 v3, v0, 27, 1
	v_lshrrev_b32_e32 v3, 22, v3
	v_add_u32_e32 v3, v2, v3
	v_and_b32_e32 v3, 0xfffffc00, v3
	v_sub_u32_e32 v2, v2, v3
	v_lshrrev_b32_e32 v3, 4, v2
	v_ashrrev_i32_e32 v4, 31, v0
	v_bitop3_b32 v2, v3, v2, 32 bitop3:0x6c
	v_lshrrev_b32_e32 v4, 26, v4
	v_ashrrev_i32_e32 v3, 31, v2
	v_add_u32_e32 v4, v0, v4
	v_lshrrev_b32_e32 v3, 26, v3
	v_ashrrev_i32_e32 v14, 6, v4
	v_add_u32_e32 v3, v2, v3
	v_lshlrev_b32_e32 v4, 3, v14
	s_add_u32 s28, s8, 0x4f00000
	v_ashrrev_i32_e32 v13, 6, v3
	v_and_b32_e32 v4, -16, v4
	s_addc_u32 s29, s9, 0
	s_ashr_i32 s10, s6, 6
	v_add_u32_e32 v4, v13, v4
	v_and_b32_e32 v5, 3, v13
	s_ashr_i32 s7, s6, 8
	s_lshl_b32 s30, s10, 10
	v_and_or_b32 v5, v4, s4, v5
	v_readlane_b32 s4, v252, 54
	v_readlane_b32 s5, v252, 55
	s_add_u32 s11, s0, s4
	v_lshrrev_b32_e32 v6, 2, v4
	v_lshlrev_b32_e32 v7, 1, v4
	v_and_b32_e32 v3, 0xc0, v3
	s_addc_u32 s12, s1, s5
	v_readlane_b32 s4, v252, 57
	v_and_b32_e32 v6, 4, v6
	v_and_b32_e32 v7, 24, v7
	v_sub_u32_e32 v2, v2, v3
	s_add_u32 s4, s28, s4
	v_or3_b32 v5, v5, v6, v7
	v_lshlrev_b32_e32 v6, 5, v14
	v_ashrrev_i16_sdwa v2, v224, sext(v2) dst_sel:DWORD dst_unused:UNUSED_PAD src0_sel:DWORD src1_sel:BYTE_0
	s_addc_u32 s5, s29, 0
	v_readlane_b32 s13, v252, 52
	v_and_b32_e32 v6, 32, v6
	v_bfe_i32 v15, v2, 0, 16
	s_add_u32 s24, s4, s13
	v_add_lshl_u32 v2, v6, v15, 1
	s_addc_u32 s25, s5, 0
	s_add_i32 s31, s30, 0
	v_lshl_add_u32 v134, v5, 12, v2
	s_add_i32 m0, s31, 0x10000
	v_lshl_add_u32 v136, v4, 13, v2
	global_load_lds_dwordx4 v134, s[24:25]
	s_add_i32 m0, s31, 0x12000
	s_add_u32 s4, s24, 0x80000
	global_load_lds_dwordx4 v130, s[24:25]
	s_addc_u32 s5, s25, 0
	s_add_i32 m0, s31, 0x14000
	v_mov_b32_e32 v135, v1
	global_load_lds_dwordx4 v134, s[4:5]
	s_add_i32 m0, s31, 0x16000
	s_add_u32 s22, s11, s13
	s_addc_u32 s23, s12, 0
	s_add_i32 s34, s31, 0x2000
	global_load_lds_dwordx4 v130, s[4:5]
	s_mov_b32 m0, s31
	s_add_u32 s4, s22, 0x100000
	global_load_lds_dwordx4 v136, s[22:23]
	s_mov_b32 m0, s34
	s_addc_u32 s5, s23, 0
	s_add_i32 s35, s31, 0x4000
	global_load_lds_dwordx4 v132, s[22:23]
	s_mov_b32 m0, s35
	s_add_i32 s38, s31, 0x6000
	global_load_lds_dwordx4 v136, s[4:5]
	s_mov_b32 m0, s38
	v_mov_b32_e32 v131, v1
	global_load_lds_dwordx4 v132, s[4:5]
	v_mov_b32_e32 v137, v1
	v_mov_b32_e32 v133, v1
	s_cmp_eq_u32 s7, 1
	v_lshl_add_u64 v[8:9], s[24:25], 0, v[134:135]
	v_lshl_add_u64 v[6:7], s[24:25], 0, v[130:131]
	v_lshl_add_u64 v[2:3], s[22:23], 0, v[136:137]
	s_cselect_b64 s[4:5], -1, 0
	s_cmp_lg_u32 s7, 1
	v_lshl_add_u64 v[4:5], s[22:23], 0, v[132:133]
	s_cbranch_scc1 .LBB0_1141
	s_barrier
